# MLA softmax row-max tree via v_max3 without canonicalising max(x,x) (41 fewer VALU per tile)
# baseline (speedup 1.0000x reference)
; template <bool MLA>
; __device__ __forceinline__ void attn_unit(const P& p, LAS unsigned char* lds, const int b, const int h, const int qb) {
;     ...
;                 float pm = -3.0e38f;
;                 if (k0 + 63 > qw) {
; #pragma unroll
;                     for (int r = 0; r < 16; ++r) { const int c = (r & 3) + 8 * (r >> 2);
;                         if (c > dq) p0[r] = -__builtin_inff(); if (c + 32 > dq) p1[r] = -__builtin_inff(); }
;                 }
; #pragma unroll
;                 for (int r = 0; r < 16; ++r) pm = fmaxf(pm, fmaxf(p0[r], p1[r]));
;                 pm = fmaxf(pm, __shfl_xor(pm, 32));
;                 const float mn = fmaxf(m_run, pm), alpha = __builtin_amdgcn_exp2f(m_run - mn); m_run = mn;
;                 float ps = 0.f;
; #pragma unroll
;                 for (int r = 0; r < 16; ++r) { p0[r] = __builtin_amdgcn_exp2f(p0[r] - mn); p1[r] = __builtin_amdgcn_exp2f(p1[r] - mn); ps += p0[r] + p1[r]; }
;                 ps += __shfl_xor(ps, 32);
;                 l_run = l_run * alpha + ps;
;                 if (__any(alpha < 1.f)) { if (hi == 0) al[r32] = alpha; asm volatile("s_waitcnt lgkmcnt(0)" ::: "memory");
; #pragma unroll
;                     for (int r = 0; r < 16; ++r) { const float a = al[(r & 3) + 8 * (r >> 2) + 4 * hi];
; #pragma unroll
;                         for (int d0 = 0; d0 < 4; ++d0) o[d0][r] *= a; } }
.LBB0_711:
	s_nop 8
	s_mov_b32 s0, 0xff61b1e6
	v_max3_f32 v3, v82, v83, s0
	v_max3_f32 v4, v84, v85, v86
	v_max3_f32 v5, v87, v88, v89
	v_max3_f32 v3, v3, v90, v91
	v_max3_f32 v4, v4, v92, v93
	v_max3_f32 v5, v5, v94, v95
	v_max3_f32 v3, v3, v96, v97
	v_max3_f32 v4, v4, v98, v99
	v_max3_f32 v5, v5, v100, v101
	v_max3_f32 v3, v3, v102, v103
	v_max3_f32 v4, v4, v104, v105
	v_max3_f32 v5, v5, v106, v107
	v_max3_f32 v3, v3, v108, v109
	v_max3_f32 v4, v4, v110, v111
	v_max3_f32 v5, v5, v112, v113
	v_max3_f32 v3, v3, v4, v5
	v_and_b32_e32 v5, 64, v211
	v_xor_b32_e32 v4, 32, v211
	v_add_u32_e32 v5, 64, v5
	v_cmp_lt_i32_e32 vcc, v4, v5
	s_nop 1
	v_cndmask_b32_e32 v4, v211, v4, vcc
	v_lshlrev_b32_e32 v217, 2, v4
	ds_bpermute_b32 v4, v217, v3
	s_waitcnt lgkmcnt(0)
	v_max3_f32 v3, v216, v3, v4
	v_sub_f32_e32 v4, v82, v3
	v_exp_f32_e32 v10, v4
	v_sub_f32_e32 v4, v98, v3
	v_exp_f32_e32 v4, v4
	v_sub_f32_e32 v5, v83, v3
	v_exp_f32_e32 v12, v5
	v_sub_f32_e32 v5, v99, v3
	v_add_f32_e32 v6, v10, v4
	v_add_f32_e32 v8, 0, v6
	v_sub_f32_e32 v6, v84, v3
	v_exp_f32_e32 v5, v5
	v_exp_f32_e32 v14, v6
	v_sub_f32_e32 v6, v100, v3
	v_exp_f32_e32 v6, v6
	v_add_f32_e32 v9, v12, v5
	v_sub_f32_e32 v7, v85, v3
	v_add_f32_e32 v8, v9, v8
	v_add_f32_e32 v9, v14, v6
	v_exp_f32_e32 v16, v7
	v_sub_f32_e32 v7, v101, v3
	v_add_f32_e32 v11, v9, v8
	v_sub_f32_e32 v8, v86, v3
	v_exp_f32_e32 v7, v7
	v_exp_f32_e32 v84, v8
	v_sub_f32_e32 v8, v102, v3
	v_exp_f32_e32 v8, v8
	v_add_f32_e32 v13, v16, v7
	v_sub_f32_e32 v9, v87, v3
	v_add_f32_e32 v11, v13, v11
	v_add_f32_e32 v13, v84, v8
	v_exp_f32_e32 v87, v9
	v_sub_f32_e32 v9, v103, v3
	v_add_f32_e32 v15, v13, v11
	v_sub_f32_e32 v11, v88, v3
	v_exp_f32_e32 v9, v9
	v_exp_f32_e32 v98, v11
	v_sub_f32_e32 v11, v104, v3
	v_exp_f32_e32 v11, v11
	v_add_f32_e32 v17, v87, v9
	v_sub_f32_e32 v13, v89, v3
	v_add_f32_e32 v15, v17, v15
	v_add_f32_e32 v17, v98, v11
	v_exp_f32_e32 v99, v13
	v_sub_f32_e32 v13, v105, v3
	v_add_f32_e32 v82, v17, v15
	v_sub_f32_e32 v15, v90, v3
	v_exp_f32_e32 v13, v13
	v_exp_f32_e32 v83, v15
	v_sub_f32_e32 v15, v106, v3
	v_exp_f32_e32 v15, v15
	v_add_f32_e32 v85, v99, v13
	v_sub_f32_e32 v17, v91, v3
	v_add_f32_e32 v82, v85, v82
	v_add_f32_e32 v85, v83, v15
	v_exp_f32_e32 v86, v17
	v_sub_f32_e32 v17, v107, v3
	v_add_f32_e32 v89, v85, v82
	v_sub_f32_e32 v82, v92, v3
	v_exp_f32_e32 v17, v17
	v_exp_f32_e32 v88, v82
	v_sub_f32_e32 v82, v108, v3
	v_exp_f32_e32 v82, v82
	v_add_f32_e32 v91, v86, v17
	v_sub_f32_e32 v85, v93, v3
	v_add_f32_e32 v89, v91, v89
	v_add_f32_e32 v91, v88, v82
	v_exp_f32_e32 v90, v85
	v_sub_f32_e32 v85, v109, v3
	v_add_f32_e32 v93, v91, v89
	v_sub_f32_e32 v89, v94, v3
	v_exp_f32_e32 v85, v85
	v_exp_f32_e32 v92, v89
	v_sub_f32_e32 v89, v110, v3
	v_exp_f32_e32 v89, v89
	v_add_f32_e32 v100, v90, v85
	v_sub_f32_e32 v91, v95, v3
	v_add_f32_e32 v93, v100, v93
	v_add_f32_e32 v95, v92, v89
	v_exp_f32_e32 v94, v91
	v_sub_f32_e32 v91, v111, v3
	v_add_f32_e32 v100, v95, v93
	v_sub_f32_e32 v93, v96, v3
	v_exp_f32_e32 v91, v91
	v_exp_f32_e32 v101, v93
	v_sub_f32_e32 v93, v112, v3
	v_sub_f32_e32 v95, v97, v3
	v_exp_f32_e32 v93, v93
	v_exp_f32_e32 v102, v95
	v_sub_f32_e32 v95, v113, v3
	v_exp_f32_e32 v95, v95
	v_add_f32_e32 v103, v94, v91
	v_add_f32_e32 v96, v103, v100
	v_add_f32_e32 v97, v101, v93
	v_add_f32_e32 v97, v97, v96
	v_add_f32_e32 v100, v102, v95
	v_sub_f32_e32 v216, v216, v3
	v_add_f32_e32 v97, v100, v97
	v_exp_f32_e32 v96, v216
	ds_bpermute_b32 v100, v217, v97
	v_cmp_gt_f32_e32 vcc, 1.0, v96
	s_cbranch_vccz .LBB0_715
	s_and_saveexec_b64 s[0:1], s[4:5]
	ds_write_b32 v212, v96
	s_or_b64 exec, exec, s[0:1]
	s_waitcnt lgkmcnt(0)
	ds_read_b128 v[104:107], v214 offset:96
	ds_read_b128 v[108:111], v214 offset:64
	ds_read_b128 v[216:219], v214 offset:32
	ds_read_b128 v[220:223], v214
	s_waitcnt lgkmcnt(3)
	v_pk_mul_f32 v[80:81], v[80:81], v[106:107]
	s_waitcnt lgkmcnt(2)
	v_pk_mul_f32 v[76:77], v[76:77], v[110:111]
	s_waitcnt lgkmcnt(1)
	v_pk_mul_f32 v[72:73], v[72:73], v[218:219]
	s_waitcnt lgkmcnt(0)
	v_pk_mul_f32 v[68:69], v[68:69], v[222:223]
	v_pk_mul_f32 v[78:79], v[78:79], v[104:105]
	v_pk_mul_f32 v[74:75], v[74:75], v[108:109]
	v_pk_mul_f32 v[70:71], v[70:71], v[216:217]
	v_pk_mul_f32 v[66:67], v[66:67], v[220:221]
	v_pk_mul_f32 v[64:65], v[64:65], v[106:107]
	v_pk_mul_f32 v[60:61], v[60:61], v[110:111]
	v_pk_mul_f32 v[56:57], v[56:57], v[218:219]
	v_pk_mul_f32 v[52:53], v[52:53], v[222:223]
	v_pk_mul_f32 v[62:63], v[62:63], v[104:105]
	v_pk_mul_f32 v[58:59], v[58:59], v[108:109]
	v_pk_mul_f32 v[54:55], v[54:55], v[216:217]
	v_pk_mul_f32 v[50:51], v[50:51], v[220:221]
	v_pk_mul_f32 v[48:49], v[48:49], v[106:107]
	v_pk_mul_f32 v[44:45], v[44:45], v[110:111]
	v_pk_mul_f32 v[40:41], v[40:41], v[218:219]
	v_pk_mul_f32 v[36:37], v[36:37], v[222:223]
	v_pk_mul_f32 v[46:47], v[46:47], v[104:105]
	v_pk_mul_f32 v[42:43], v[42:43], v[108:109]
	v_pk_mul_f32 v[38:39], v[38:39], v[216:217]
	v_pk_mul_f32 v[34:35], v[34:35], v[220:221]
	v_pk_mul_f32 v[32:33], v[32:33], v[106:107]
	v_pk_mul_f32 v[28:29], v[28:29], v[110:111]
	v_pk_mul_f32 v[24:25], v[24:25], v[218:219]
	v_pk_mul_f32 v[20:21], v[20:21], v[222:223]
	v_pk_mul_f32 v[30:31], v[30:31], v[104:105]
	v_pk_mul_f32 v[26:27], v[26:27], v[108:109]
	v_pk_mul_f32 v[22:23], v[22:23], v[216:217]
	v_pk_mul_f32 v[18:19], v[18:19], v[220:221]

; template <bool MLA>
; __device__ __forceinline__ void attn_unit(const P& p, LAS unsigned char* lds, const int b, const int h, const int qb) {
;     ...
;                 float pm = -3.0e38f;
;                 if (k0 + 63 > qw) {
; #pragma unroll
;                     for (int r = 0; r < 16; ++r) { const int c = (r & 3) + 8 * (r >> 2);
;                         if (c > dq) p0[r] = -__builtin_inff(); if (c + 32 > dq) p1[r] = -__builtin_inff(); }
;                 }
; #pragma unroll
;                 for (int r = 0; r < 16; ++r) pm = fmaxf(pm, fmaxf(p0[r], p1[r]));
;                 pm = fmaxf(pm, __shfl_xor(pm, 32));
;                 const float mn = fmaxf(m_run, pm), alpha = __builtin_amdgcn_exp2f(m_run - mn); m_run = mn;
;                 float ps = 0.f;
; #pragma unroll
;                 for (int r = 0; r < 16; ++r) { p0[r] = __builtin_amdgcn_exp2f(p0[r] - mn); p1[r] = __builtin_amdgcn_exp2f(p1[r] - mn); ps += p0[r] + p1[r]; }
;                 ps += __shfl_xor(ps, 32);
;                 l_run = l_run * alpha + ps;
;                 if (__any(alpha < 1.f)) { if (hi == 0) al[r32] = alpha; asm volatile("s_waitcnt lgkmcnt(0)" ::: "memory");
; #pragma unroll
;                     for (int r = 0; r < 16; ++r) { const float a = al[(r & 3) + 8 * (r >> 2) + 4 * hi];
; #pragma unroll
;                         for (int d0 = 0; d0 < 4; ++d0) o[d0][r] *= a; } }
.LBB0_877:
	s_nop 8
	s_mov_b32 s0, 0xff61b1e6
	v_max3_f32 v3, v82, v83, s0
	v_max3_f32 v4, v84, v85, v86
	v_max3_f32 v5, v87, v88, v89
	v_max3_f32 v3, v3, v90, v91
	v_max3_f32 v4, v4, v92, v93
	v_max3_f32 v5, v5, v94, v95
	v_max3_f32 v3, v3, v96, v97
	v_max3_f32 v4, v4, v98, v99
	v_max3_f32 v5, v5, v100, v101
	v_max3_f32 v3, v3, v102, v103
	v_max3_f32 v4, v4, v104, v105
	v_max3_f32 v5, v5, v106, v107
	v_max3_f32 v3, v3, v108, v109
	v_max3_f32 v4, v4, v110, v111
	v_max3_f32 v5, v5, v112, v113
	v_max3_f32 v3, v3, v4, v5
	v_and_b32_e32 v5, 64, v214
	v_xor_b32_e32 v4, 32, v214
	v_add_u32_e32 v5, 64, v5
	v_cmp_lt_i32_e32 vcc, v4, v5
	s_nop 1
	v_cndmask_b32_e32 v4, v214, v4, vcc
	v_lshlrev_b32_e32 v220, 2, v4
	ds_bpermute_b32 v4, v220, v3
	s_waitcnt lgkmcnt(0)
	v_max3_f32 v3, v219, v3, v4
	v_sub_f32_e32 v4, v82, v3
	v_exp_f32_e32 v10, v4
	v_sub_f32_e32 v4, v98, v3
	v_exp_f32_e32 v4, v4
	v_sub_f32_e32 v5, v83, v3
	v_exp_f32_e32 v12, v5
	v_sub_f32_e32 v5, v99, v3
	v_add_f32_e32 v6, v10, v4
	v_add_f32_e32 v8, 0, v6
	v_sub_f32_e32 v6, v84, v3
	v_exp_f32_e32 v5, v5
	v_exp_f32_e32 v14, v6
	v_sub_f32_e32 v6, v100, v3
	v_exp_f32_e32 v6, v6
	v_add_f32_e32 v9, v12, v5
	v_sub_f32_e32 v7, v85, v3
	v_add_f32_e32 v8, v9, v8
	v_add_f32_e32 v9, v14, v6
	v_exp_f32_e32 v16, v7
	v_sub_f32_e32 v7, v101, v3
	v_add_f32_e32 v11, v9, v8
	v_sub_f32_e32 v8, v86, v3
	v_exp_f32_e32 v7, v7
	v_exp_f32_e32 v84, v8
	v_sub_f32_e32 v8, v102, v3
	v_exp_f32_e32 v8, v8
	v_add_f32_e32 v13, v16, v7
	v_sub_f32_e32 v9, v87, v3
	v_add_f32_e32 v11, v13, v11
	v_add_f32_e32 v13, v84, v8
	v_exp_f32_e32 v87, v9
	v_sub_f32_e32 v9, v103, v3
	v_add_f32_e32 v15, v13, v11
	v_sub_f32_e32 v11, v88, v3
	v_exp_f32_e32 v9, v9
	v_exp_f32_e32 v98, v11
	v_sub_f32_e32 v11, v104, v3
	v_exp_f32_e32 v11, v11
	v_add_f32_e32 v17, v87, v9
	v_sub_f32_e32 v13, v89, v3
	v_add_f32_e32 v15, v17, v15
	v_add_f32_e32 v17, v98, v11
	v_exp_f32_e32 v99, v13
	v_sub_f32_e32 v13, v105, v3
	v_add_f32_e32 v82, v17, v15
	v_sub_f32_e32 v15, v90, v3
	v_exp_f32_e32 v13, v13
	v_exp_f32_e32 v83, v15
	v_sub_f32_e32 v15, v106, v3
	v_exp_f32_e32 v15, v15
	v_add_f32_e32 v85, v99, v13
	v_sub_f32_e32 v17, v91, v3
	v_add_f32_e32 v82, v85, v82
	v_add_f32_e32 v85, v83, v15
	v_exp_f32_e32 v86, v17
	v_sub_f32_e32 v17, v107, v3
	v_add_f32_e32 v89, v85, v82
	v_sub_f32_e32 v82, v92, v3
	v_exp_f32_e32 v17, v17
	v_exp_f32_e32 v88, v82
	v_sub_f32_e32 v82, v108, v3
	v_exp_f32_e32 v82, v82
	v_add_f32_e32 v91, v86, v17
	v_sub_f32_e32 v85, v93, v3
	v_add_f32_e32 v89, v91, v89
	v_add_f32_e32 v91, v88, v82
	v_exp_f32_e32 v90, v85
	v_sub_f32_e32 v85, v109, v3
	v_add_f32_e32 v93, v91, v89
	v_sub_f32_e32 v89, v94, v3
	v_exp_f32_e32 v85, v85
	v_exp_f32_e32 v92, v89
	v_sub_f32_e32 v89, v110, v3
	v_exp_f32_e32 v89, v89
	v_add_f32_e32 v100, v90, v85
	v_sub_f32_e32 v91, v95, v3
	v_add_f32_e32 v93, v100, v93
	v_add_f32_e32 v95, v92, v89
	v_exp_f32_e32 v94, v91
	v_sub_f32_e32 v91, v111, v3
	v_add_f32_e32 v100, v95, v93
	v_sub_f32_e32 v93, v96, v3
	v_exp_f32_e32 v91, v91
	v_exp_f32_e32 v101, v93
	v_sub_f32_e32 v93, v112, v3
	v_sub_f32_e32 v95, v97, v3
	v_exp_f32_e32 v93, v93
	v_exp_f32_e32 v102, v95
	v_sub_f32_e32 v95, v113, v3
	v_exp_f32_e32 v95, v95
	v_add_f32_e32 v103, v94, v91
	v_add_f32_e32 v96, v103, v100
	v_add_f32_e32 v97, v101, v93
	v_add_f32_e32 v97, v97, v96
	v_add_f32_e32 v100, v102, v95
	v_sub_f32_e32 v219, v219, v3
	v_add_f32_e32 v97, v100, v97
	v_exp_f32_e32 v96, v219
	ds_bpermute_b32 v100, v220, v97
	v_cmp_gt_f32_e32 vcc, 1.0, v96
	s_cbranch_vccz .LBB0_881
	s_and_saveexec_b64 s[0:1], s[4:5]
	ds_write_b32 v215, v96
	s_or_b64 exec, exec, s[0:1]
	s_waitcnt lgkmcnt(0)
	ds_read_b128 v[104:107], v217 offset:96
	ds_read_b128 v[108:111], v217 offset:64
	ds_read_b128 v[220:223], v217 offset:32
	ds_read_b128 v[224:227], v217
	s_waitcnt lgkmcnt(3)
	v_pk_mul_f32 v[80:81], v[80:81], v[106:107]
	s_waitcnt lgkmcnt(2)
	v_pk_mul_f32 v[76:77], v[76:77], v[110:111]
	s_waitcnt lgkmcnt(1)
	v_pk_mul_f32 v[72:73], v[72:73], v[222:223]
	s_waitcnt lgkmcnt(0)
	v_pk_mul_f32 v[68:69], v[68:69], v[226:227]
	v_pk_mul_f32 v[78:79], v[78:79], v[104:105]
	v_pk_mul_f32 v[74:75], v[74:75], v[108:109]
	v_pk_mul_f32 v[70:71], v[70:71], v[220:221]
	v_pk_mul_f32 v[66:67], v[66:67], v[224:225]
	v_pk_mul_f32 v[64:65], v[64:65], v[106:107]
	v_pk_mul_f32 v[60:61], v[60:61], v[110:111]
	v_pk_mul_f32 v[56:57], v[56:57], v[222:223]
	v_pk_mul_f32 v[52:53], v[52:53], v[226:227]
	v_pk_mul_f32 v[62:63], v[62:63], v[104:105]
	v_pk_mul_f32 v[58:59], v[58:59], v[108:109]
	v_pk_mul_f32 v[54:55], v[54:55], v[220:221]
	v_pk_mul_f32 v[50:51], v[50:51], v[224:225]
	v_pk_mul_f32 v[48:49], v[48:49], v[106:107]
	v_pk_mul_f32 v[44:45], v[44:45], v[110:111]
	v_pk_mul_f32 v[40:41], v[40:41], v[222:223]
	v_pk_mul_f32 v[36:37], v[36:37], v[226:227]
	v_pk_mul_f32 v[46:47], v[46:47], v[104:105]
	v_pk_mul_f32 v[42:43], v[42:43], v[108:109]
	v_pk_mul_f32 v[38:39], v[38:39], v[220:221]
	v_pk_mul_f32 v[34:35], v[34:35], v[224:225]
	v_pk_mul_f32 v[32:33], v[32:33], v[106:107]
	v_pk_mul_f32 v[28:29], v[28:29], v[110:111]
	v_pk_mul_f32 v[24:25], v[24:25], v[222:223]
	v_pk_mul_f32 v[20:21], v[20:21], v[226:227]
	v_pk_mul_f32 v[30:31], v[30:31], v[104:105]
	v_pk_mul_f32 v[26:27], v[26:27], v[108:109]
	v_pk_mul_f32 v[22:23], v[22:23], v[220:221]
	v_pk_mul_f32 v[18:19], v[18:19], v[224:225]
